# v13 = v9 + naattn tile loops hand-pipelined: K fragments prefetched one tile ahead, 16 bias LDS reads batched, bias-table copy single wait
# speedup vs baseline: 1.0191x; 1.0191x over previous
; __device__ __forceinline__ void ph_naattn(const Params& p, float* lds, int wg, int nwg) {
;     ...
;     for (int u = wg * 8 + wave; u < 4096 + 256; u += nwg * 8) {
;         int b, h, qrow0, nband = 0, gr = 0, r0 = 0, q0 = 0;
;         if (u < 4096) { h = u & 15; int x = u >> 4; q0 = (x & 1) * 32; x >>= 1; gr = x & 63; b = x >> 6; qrow0 = b * TL + gr * 64 + q0; r0 = gr - 4; r0 = r0 < 0 ? 0 : (r0 > 56 ? 56 : r0); nband = 8; }
;         else { int x = u - 4096; h = x & 15; x >>= 4; b = x >> 3; qrow0 = NL + b * TC + (x & 7) * 32; }
;         if (nband) for (int i = lane; i < 465; i += 64) tab[i] = p.in[22][h * 465 + i];
.LBB0_757:
	v_cndmask_b32_e64 v2, 0, 1, s[8:9]
	v_cmp_ne_u32_e64 s[4:5], 1, v2
	s_andn2_b64 vcc, exec, s[8:9]
	s_and_b32 s15, s2, 15
	s_cbranch_vccnz .LBB0_761
	s_mul_i32 s8, s15, 0x1d1
	v_readlane_b32 s56, v246, 32
	v_add_lshl_u32 v2, v69, s8, 2
	v_readlane_b32 s68, v246, 44
	v_readlane_b32 s69, v246, 45
	s_nop 4
	global_load_dword v3, v2, s[68:69]
	global_load_dword v4, v2, s[68:69] offset:256
	global_load_dword v200, v2, s[68:69] offset:512
	global_load_dword v201, v2, s[68:69] offset:768
	global_load_dword v202, v2, s[68:69] offset:1024
	global_load_dword v203, v2, s[68:69] offset:1280
	global_load_dword v204, v2, s[68:69] offset:1536
	v_readlane_b32 s57, v246, 33
	v_readlane_b32 s58, v246, 34
	v_readlane_b32 s59, v246, 35
	v_readlane_b32 s60, v246, 36
	v_readlane_b32 s61, v246, 37
	v_readlane_b32 s62, v246, 38
	v_readlane_b32 s63, v246, 39
	v_readlane_b32 s64, v246, 40
	v_readlane_b32 s65, v246, 41
	v_readlane_b32 s66, v246, 42
	v_readlane_b32 s67, v246, 43
	v_readlane_b32 s70, v246, 46
	v_readlane_b32 s71, v246, 47
	s_waitcnt vmcnt(0)
	ds_write2st64_b32 v85, v3, v4 offset1:1
	ds_write2st64_b32 v85, v200, v201 offset0:2 offset1:3
	ds_write2st64_b32 v85, v202, v203 offset0:4 offset1:5
	ds_write_b32 v85, v204 offset:1536
	s_and_saveexec_b64 s[8:9], s[0:1]
	s_cbranch_execz .LBB0_760
	v_readlane_b32 s56, v246, 32
	v_mov_b32_e32 v3, v67
	v_readlane_b32 s68, v246, 44
	v_readlane_b32 s69, v246, 45
	v_readlane_b32 s57, v246, 33
	v_readlane_b32 s58, v246, 34
	v_lshl_add_u64 v[2:3], s[68:69], 0, v[2:3]
	global_load_dword v2, v[2:3], off offset:1792
	v_readlane_b32 s59, v246, 35
	v_readlane_b32 s60, v246, 36
	v_readlane_b32 s61, v246, 37
	v_readlane_b32 s62, v246, 38
	v_readlane_b32 s63, v246, 39
	v_readlane_b32 s64, v246, 40
	v_readlane_b32 s65, v246, 41
	v_readlane_b32 s66, v246, 42
	v_readlane_b32 s67, v246, 43
	v_readlane_b32 s70, v246, 46
	v_readlane_b32 s71, v246, 47
	s_waitcnt vmcnt(0)
	ds_write_b32 v85, v2 offset:1792

; template <bool BAND> ...
;     pg8::bf16x8 kf[4];
; #pragma unroll
;     for (int ks = 0; ks < 4; ++ks) kf[ks] = *(const pg8::bf16x8*)(p.Kb + ((size_t)keyrow0 * 4 + ks) * 512 + (hh * 32 + r) * 8);
;     pg8::bf16x8 vf[2][2];
; #pragma unroll
;     for (int nt = 0; nt < 2; ++nt)
; #pragma unroll
;         for (int s = 0; s < 2; ++s) vf[nt][s] = *(const pg8::bf16x8*)(vtp + ((nt * 2 + s) * 64 + hh * 32 + r) * 8);
;     f32x16 sacc;
; #pragma unroll
;     for (int i = 0; i < 16; ++i) sacc[i] = 0.f;
; #pragma unroll
;     for (int ks = 0; ks < 4; ++ks) sacc = __builtin_amdgcn_mfma_f32_32x32x16_bf16(kf[ks], qf[ks], sacc, 0, 0, 0);
;     float pv[16];
; #pragma unroll
;     for (int reg = 0; reg < 16; ++reg) {
;         float sc = sacc[reg];
;         if (BAND) {
;             const int kc = kc0 + (reg & 3) + 8 * (reg >> 2) + 4 * hh;
;             const bool valid = (unsigned)(kc - c0) < 16u;
;             const int bi = valid ? browoff + kc - q + 15 : 0;
;             sc += tab[bi];
;             pv[reg] = valid ? __builtin_amdgcn_exp2f(sc * 1.44269504f - mq) : 0.f;
; __device__ __forceinline__ void ph_naattn(const Params& p, float* lds, int wg, int nwg) {
;     ...
;         pg8::bf16x8 qf[4];
; #pragma unroll
;         for (int ks = 0; ks < 4; ++ks) qf[ks] = *(const pg8::bf16x8*)(p.Qb + (size_t)(qrow0 + r) * 1024 + h * 64 + 16 * ks + 8 * hh);
;         const float mq = p.QM[(qrow0 + r) * 16 + h];
;         f32x16 o0, o1;
; #pragma unroll
;         for (int i = 0; i < 16; ++i) { o0[i] = 0.f; o1[i] = 0.f; }
;         float l = 0.f;
;         const int q = q0 + r; int c0 = q - 8; c0 = c0 < 0 ? 0 : (c0 > 48 ? 48 : c0);
;         for (int tl = 0; tl < nband * 2; ++tl) {
;             const int i = tl >> 1, kt = tl & 1;
;             { const int tid_ = (b * 16 + h) * 136 + (r0 + i) * 2 + kt; na_tile<true>(p, tab, qf, tid_, p.VTl + (size_t)tid_ * 2048, TL, h, r, hh, 32 * kt, q, c0, (r0 + i - gr + 7) * 31, mq, o0, o1, l); }
.LBB0_761:
	v_add_u32_e32 v78, s6, v84
	v_ashrrev_i32_e32 v79, 31, v78
	v_lshlrev_b64 v[2:3], 11, v[78:79]
	v_lshl_add_u64 v[2:3], s[54:55], 0, v[2:3]
	s_lshl_b32 s6, s15, 7
	v_lshl_add_u64 v[2:3], v[2:3], 0, s[6:7]
	v_lshl_add_u64 v[2:3], v[2:3], 0, v[76:77]
	global_load_dwordx4 v[50:53], v[2:3], off
	global_load_dwordx4 v[54:57], v[2:3], off offset:32
	global_load_dwordx4 v[58:61], v[2:3], off offset:64
	global_load_dwordx4 v[62:65], v[2:3], off offset:96
	v_lshl_or_b32 v2, v78, 4, s15
	v_readlane_b32 s56, v248, 9
	v_ashrrev_i32_e32 v3, 31, v2
	v_readlane_b32 s57, v248, 10
	s_and_b64 vcc, exec, s[4:5]
	s_mov_b32 s4, 0
	v_lshl_add_u64 v[2:3], v[2:3], 2, s[56:57]
	global_load_dword v86, v[2:3], off
	v_readlane_b32 s58, v248, 11
	v_readlane_b32 s59, v248, 12
	v_readlane_b32 s60, v248, 13
	v_readlane_b32 s61, v248, 14
	v_readlane_b32 s62, v248, 15
	v_readlane_b32 s63, v248, 16
	v_readlane_b32 s64, v248, 17
	v_readlane_b32 s65, v248, 18
	v_readlane_b32 s66, v248, 19
	v_readlane_b32 s67, v248, 20
	v_readlane_b32 s68, v248, 21
	v_readlane_b32 s69, v248, 22
	v_readlane_b32 s70, v248, 23
	v_readlane_b32 s71, v248, 24
	s_cbranch_vccnz .LBB0_764
	v_or_b32_e32 v80, s17, v84
	s_lshl_b32 s5, s12, 4
	v_med3_i32 v2, v80, 8, 56
	s_or_b32 s5, s5, s15
	v_mov_b32_e32 v87, 0
	v_add_u32_e32 v81, -8, v2
	s_mulk_i32 s5, 0x88
	v_mov_b32_e32 v2, 0
	v_mov_b32_e32 v3, v87
	v_mov_b32_e32 v4, v87
	v_mov_b32_e32 v5, v87
	v_mov_b32_e32 v6, v87
	v_mov_b32_e32 v7, v87
	v_mov_b32_e32 v8, v87
	v_mov_b32_e32 v9, v87
	v_mov_b32_e32 v10, v87
	v_mov_b32_e32 v11, v87
	v_mov_b32_e32 v12, v87
	v_mov_b32_e32 v13, v87
	v_mov_b32_e32 v14, v87
	v_mov_b32_e32 v15, v87
	v_mov_b32_e32 v16, v87
	v_mov_b32_e32 v17, v87
	v_mov_b32_e32 v18, 0
	v_mov_b32_e32 v19, v87
	v_mov_b32_e32 v20, v87
	v_mov_b32_e32 v21, v87
	v_mov_b32_e32 v22, v87
	v_mov_b32_e32 v23, v87
	v_mov_b32_e32 v24, v87
	v_mov_b32_e32 v25, v87
	v_mov_b32_e32 v26, v87
	v_mov_b32_e32 v27, v87
	v_mov_b32_e32 v28, v87
	v_mov_b32_e32 v29, v87
	v_mov_b32_e32 v30, v87
	v_mov_b32_e32 v31, v87
	v_mov_b32_e32 v32, v87
	v_mov_b32_e32 v33, v87
	s_lshl_b32 s8, s16, 1
	s_add_i32 s8, s8, s5
	s_ashr_i32 s9, s8, 31
	s_lshl_b64 s[8:9], s[8:9], 12
	v_lshl_add_u64 v[198:199], v[70:71], 0, s[8:9]
	global_load_dwordx4 v[116:119], v[198:199], off
	global_load_dwordx4 v[120:123], v[198:199], off offset:1024
	global_load_dwordx4 v[124:127], v[198:199], off offset:2048
	global_load_dwordx4 v[128:131], v[198:199], off offset:3072
.LBB0_763:
	s_lshr_b32 s6, s4, 1
	s_add_i32 s6, s6, s16
	s_lshl_b32 s8, s6, 1
	s_and_b32 s17, s4, 1
	s_add_i32 s8, s8, s5
	s_or_b32 s8, s8, s17
	s_ashr_i32 s9, s8, 31
	s_lshl_b64 s[8:9], s[8:9], 12
	v_lshl_add_u64 v[38:39], v[72:73], 0, s[8:9]
	global_load_dwordx4 v[100:103], v[38:39], off
	global_load_dwordx4 v[104:107], v[38:39], off offset:1024
	global_load_dwordx4 v[108:111], v[38:39], off offset:2048
	global_load_dwordx4 v[112:115], v[38:39], off offset:3072
	s_sub_i32 s6, s6, s13
	s_mul_i32 s6, s6, 31
	v_lshl_or_b32 v82, s17, 5, v68
	v_sub_u32_e32 v83, s6, v80
	v_add_u32_e32 v83, 0xe8, v83
	v_or_b32_e32 v133, 1, v82
	v_or_b32_e32 v134, 2, v82
	v_or_b32_e32 v135, 3, v82
	v_or_b32_e32 v136, 8, v82
	v_or_b32_e32 v137, 9, v82
	v_or_b32_e32 v138, 10, v82
	v_or_b32_e32 v139, 11, v82
	v_or_b32_e32 v140, 16, v82
	v_or_b32_e32 v141, 17, v82
	v_or_b32_e32 v142, 18, v82
	v_or_b32_e32 v143, 19, v82
	v_or_b32_e32 v144, 24, v82
	v_or_b32_e32 v145, 25, v82
	v_or_b32_e32 v146, 26, v82
	v_or_b32_e32 v147, 27, v82
	v_sub_u32_e32 v166, v82, v81
	v_sub_u32_e32 v167, v133, v81
	v_sub_u32_e32 v168, v134, v81
	v_sub_u32_e32 v169, v135, v81
	v_sub_u32_e32 v170, v136, v81
	v_sub_u32_e32 v171, v137, v81
	v_sub_u32_e32 v172, v138, v81
	v_sub_u32_e32 v173, v139, v81
	v_sub_u32_e32 v174, v140, v81
	v_sub_u32_e32 v175, v141, v81
	v_sub_u32_e32 v176, v142, v81
	v_sub_u32_e32 v177, v143, v81
	v_sub_u32_e32 v178, v144, v81
	v_sub_u32_e32 v179, v145, v81
	v_sub_u32_e32 v180, v146, v81
	v_sub_u32_e32 v181, v147, v81
	v_add_u32_e32 v132, v83, v82
	v_add_u32_e32 v133, v83, v133
	v_add_u32_e32 v134, v83, v134
	v_add_u32_e32 v135, v83, v135
	v_add_u32_e32 v136, v83, v136
	v_add_u32_e32 v137, v83, v137
	v_add_u32_e32 v138, v83, v138
	v_add_u32_e32 v139, v83, v139
	v_add_u32_e32 v140, v83, v140
	v_add_u32_e32 v141, v83, v141
	v_add_u32_e32 v142, v83, v142
	v_add_u32_e32 v143, v83, v143
	v_add_u32_e32 v144, v83, v144
	v_add_u32_e32 v145, v83, v145
	v_add_u32_e32 v146, v83, v146
	v_add_u32_e32 v147, v83, v147
	v_cmp_gt_u32_e64 s[28:29], 16, v166
	v_cmp_gt_u32_e64 s[30:31], 16, v167
	v_cmp_gt_u32_e64 s[32:33], 16, v168
	v_cmp_gt_u32_e64 s[36:37], 16, v169
	v_cmp_gt_u32_e64 s[46:47], 16, v170
	v_cmp_gt_u32_e64 s[48:49], 16, v171
	v_cmp_gt_u32_e64 s[72:73], 16, v172
	v_cmp_gt_u32_e64 s[74:75], 16, v173
	v_cmp_gt_u32_e64 s[76:77], 16, v174
	v_cmp_gt_u32_e64 s[78:79], 16, v175
	v_cmp_gt_u32_e64 s[80:81], 16, v176
	v_cmp_gt_u32_e64 s[82:83], 16, v177
	v_cmp_gt_u32_e64 s[84:85], 16, v178
	v_cmp_gt_u32_e64 s[86:87], 16, v179
	v_cmp_gt_u32_e64 s[94:95], 16, v180
	v_cmp_gt_u32_e32 vcc, 16, v181
	v_cndmask_b32_e64 v132, 0, v132, s[28:29]
	v_cndmask_b32_e64 v133, 0, v133, s[30:31]
	v_cndmask_b32_e64 v134, 0, v134, s[32:33]
	v_cndmask_b32_e64 v135, 0, v135, s[36:37]
	v_cndmask_b32_e64 v136, 0, v136, s[46:47]
	v_cndmask_b32_e64 v137, 0, v137, s[48:49]
	v_cndmask_b32_e64 v138, 0, v138, s[72:73]
	v_cndmask_b32_e64 v139, 0, v139, s[74:75]
	v_cndmask_b32_e64 v140, 0, v140, s[76:77]
	v_cndmask_b32_e64 v141, 0, v141, s[78:79]
	v_cndmask_b32_e64 v142, 0, v142, s[80:81]
	v_cndmask_b32_e64 v143, 0, v143, s[82:83]
	v_cndmask_b32_e64 v144, 0, v144, s[84:85]
	v_cndmask_b32_e64 v145, 0, v145, s[86:87]
	v_cndmask_b32_e64 v146, 0, v146, s[94:95]
	v_cndmask_b32_e32 v147, 0, v147, vcc
	v_lshl_add_u32 v132, v132, 2, s3
	v_lshl_add_u32 v133, v133, 2, s3
	v_lshl_add_u32 v134, v134, 2, s3
	v_lshl_add_u32 v135, v135, 2, s3
	v_lshl_add_u32 v136, v136, 2, s3
	v_lshl_add_u32 v137, v137, 2, s3
	v_lshl_add_u32 v138, v138, 2, s3
	v_lshl_add_u32 v139, v139, 2, s3
	v_lshl_add_u32 v140, v140, 2, s3
	v_lshl_add_u32 v141, v141, 2, s3
	v_lshl_add_u32 v142, v142, 2, s3
	v_lshl_add_u32 v143, v143, 2, s3
	v_lshl_add_u32 v144, v144, 2, s3
	v_lshl_add_u32 v145, v145, 2, s3
	v_lshl_add_u32 v146, v146, 2, s3
	v_lshl_add_u32 v147, v147, 2, s3
	ds_read_b32 v132, v132
	ds_read_b32 v133, v133
	ds_read_b32 v134, v134
	ds_read_b32 v135, v135
	ds_read_b32 v136, v136
	ds_read_b32 v137, v137
	ds_read_b32 v138, v138
	ds_read_b32 v139, v139
	ds_read_b32 v140, v140
	ds_read_b32 v141, v141
	ds_read_b32 v142, v142
	ds_read_b32 v143, v143
	ds_read_b32 v144, v144
	ds_read_b32 v145, v145
	ds_read_b32 v146, v146
	ds_read_b32 v147, v147
	s_waitcnt vmcnt(7)
; __device__ __forceinline__ unsigned cvt_pk_bf16(float lo, float hi) { const f32x2_t v = {lo, hi}; return __builtin_bit_cast(unsigned, __builtin_convertvector(v, bf16x2_t)); }
; template <bool BAND> ...
;     pg8::bf16x8 kf[4];
; #pragma unroll
;     for (int ks = 0; ks < 4; ++ks) kf[ks] = *(const pg8::bf16x8*)(p.Kb + ((size_t)keyrow0 * 4 + ks) * 512 + (hh * 32 + r) * 8);
;     pg8::bf16x8 vf[2][2];
; #pragma unroll
;     for (int nt = 0; nt < 2; ++nt)
; #pragma unroll
;         for (int s = 0; s < 2; ++s) vf[nt][s] = *(const pg8::bf16x8*)(vtp + ((nt * 2 + s) * 64 + hh * 32 + r) * 8);
;     f32x16 sacc;
; #pragma unroll
;     for (int i = 0; i < 16; ++i) sacc[i] = 0.f;
; #pragma unroll
;     for (int ks = 0; ks < 4; ++ks) sacc = __builtin_amdgcn_mfma_f32_32x32x16_bf16(kf[ks], qf[ks], sacc, 0, 0, 0);
;     float pv[16];
; #pragma unroll
;     for (int reg = 0; reg < 16; ++reg) {
;         float sc = sacc[reg];
;         if (BAND) {
;             const int kc = kc0 + (reg & 3) + 8 * (reg >> 2) + 4 * hh;
;             const bool valid = (unsigned)(kc - c0) < 16u;
;             const int bi = valid ? browoff + kc - q + 15 : 0;
;             sc += tab[bi];
;             pv[reg] = valid ? __builtin_amdgcn_exp2f(sc * 1.44269504f - mq) : 0.f;
;         } else pv[reg] = __builtin_amdgcn_exp2f(sc * 1.44269504f - mq);
;         l += pv[reg];
;     }
;     pg8::bf16x8 pf[2];
; #pragma unroll
;     for (int s = 0; s < 2; ++s) { const pg8::u32x4 w = {cvt_pk_bf16(pv[8 * s], pv[8 * s + 1]), cvt_pk_bf16(pv[8 * s + 2], pv[8 * s + 3]), cvt_pk_bf16(pv[8 * s + 4], pv[8 * s + 5]), cvt_pk_bf16(pv[8 * s + 6], pv[8 * s + 7])};
;         pf[s] = __builtin_bit_cast(pg8::bf16x8, w); }
; #pragma unroll
;     for (int s = 0; s < 2; ++s) { o0 = __builtin_amdgcn_mfma_f32_32x32x16_bf16(vf[0][s], pf[s], o0, 0, 0, 0); o1 = __builtin_amdgcn_mfma_f32_32x32x16_bf16(vf[1][s], pf[s], o1, 0, 0, 0); }
	v_mfma_f32_32x32x16_bf16 v[34:49], v[116:119], v[50:53], 0
	s_waitcnt vmcnt(6)
	v_mfma_f32_32x32x16_bf16 v[34:49], v[120:123], v[54:57], v[34:49]
	s_waitcnt vmcnt(5)
	v_mfma_f32_32x32x16_bf16 v[34:49], v[124:127], v[58:61], v[34:49]
	s_waitcnt vmcnt(4)
	v_mfma_f32_32x32x16_bf16 v[34:49], v[128:131], v[62:65], v[34:49]
	s_add_i32 s4, s4, 1
	s_lshr_b32 s6, s4, 1
	s_add_i32 s6, s6, s16
	s_lshl_b32 s8, s6, 1
	s_and_b32 s17, s4, 1
	s_add_i32 s8, s8, s5
	s_or_b32 s8, s8, s17
	s_add_i32 s6, s5, 0x80
	s_cmp_eq_u32 s14, s4
	s_cselect_b32 s8, s6, s8
	s_ashr_i32 s9, s8, 31
	s_lshl_b64 s[8:9], s[8:9], 12
	v_lshl_add_u64 v[198:199], v[70:71], 0, s[8:9]
	global_load_dwordx4 v[116:119], v[198:199], off
	global_load_dwordx4 v[120:123], v[198:199], off offset:1024
	global_load_dwordx4 v[124:127], v[198:199], off offset:2048
	global_load_dwordx4 v[128:131], v[198:199], off offset:3072
	s_waitcnt lgkmcnt(0)
	v_add_f32_e32 v34, v34, v132
	v_add_f32_e32 v35, v35, v133
	v_fma_f32 v34, v34, s11, -v86
	v_add_f32_e32 v36, v36, v134
	v_fma_f32 v35, v35, s11, -v86
	v_exp_f32_e32 v34, v34
	v_add_f32_e32 v37, v37, v135
	v_fma_f32 v36, v36, s11, -v86
	v_exp_f32_e32 v35, v35
	v_add_f32_e32 v38, v38, v136
	v_fma_f32 v37, v37, s11, -v86
	v_exp_f32_e32 v36, v36
	v_cndmask_b32_e64 v34, 0, v34, s[28:29]
	v_add_f32_e32 v39, v39, v137
	v_fma_f32 v38, v38, s11, -v86
	v_exp_f32_e32 v37, v37
	v_cndmask_b32_e64 v35, 0, v35, s[30:31]
	v_add_f32_e32 v87, v87, v34
	v_add_f32_e32 v40, v40, v138
	v_fma_f32 v39, v39, s11, -v86
	v_exp_f32_e32 v38, v38
	v_cndmask_b32_e64 v36, 0, v36, s[32:33]
	v_add_f32_e32 v87, v87, v35
	v_cvt_pk_bf16_f32 v190, v34, v35
	v_add_f32_e32 v41, v41, v139
	v_fma_f32 v40, v40, s11, -v86
	v_exp_f32_e32 v39, v39
	v_cndmask_b32_e64 v37, 0, v37, s[36:37]
	v_add_f32_e32 v87, v87, v36
	v_add_f32_e32 v42, v42, v140
	v_fma_f32 v41, v41, s11, -v86
	v_exp_f32_e32 v40, v40
	v_cndmask_b32_e64 v38, 0, v38, s[46:47]
	v_add_f32_e32 v87, v87, v37
	v_cvt_pk_bf16_f32 v191, v36, v37
	v_add_f32_e32 v43, v43, v141
	v_fma_f32 v42, v42, s11, -v86
	v_exp_f32_e32 v41, v41
	v_cndmask_b32_e64 v39, 0, v39, s[48:49]
	v_add_f32_e32 v87, v87, v38
	v_add_f32_e32 v44, v44, v142
	v_fma_f32 v43, v43, s11, -v86
	v_exp_f32_e32 v42, v42
	v_cndmask_b32_e64 v40, 0, v40, s[72:73]
	v_add_f32_e32 v87, v87, v39
	v_cvt_pk_bf16_f32 v192, v38, v39
	v_add_f32_e32 v45, v45, v143
	v_fma_f32 v44, v44, s11, -v86
	v_exp_f32_e32 v43, v43
	v_cndmask_b32_e64 v41, 0, v41, s[74:75]
	v_add_f32_e32 v87, v87, v40
	v_add_f32_e32 v46, v46, v144
	v_fma_f32 v45, v45, s11, -v86
	v_exp_f32_e32 v44, v44
	v_cndmask_b32_e64 v42, 0, v42, s[76:77]
	v_add_f32_e32 v87, v87, v41
	v_cvt_pk_bf16_f32 v193, v40, v41
	v_add_f32_e32 v47, v47, v145
	v_fma_f32 v46, v46, s11, -v86
	v_exp_f32_e32 v45, v45
	v_cndmask_b32_e64 v43, 0, v43, s[78:79]
	v_add_f32_e32 v87, v87, v42
	s_waitcnt vmcnt(7)
	v_mfma_f32_32x32x16_bf16 v[2:17], v[100:103], v[190:193], v[2:17]
	s_waitcnt vmcnt(5)
	v_mfma_f32_32x32x16_bf16 v[18:33], v[108:111], v[190:193], v[18:33]
	v_add_f32_e32 v48, v48, v146
	v_fma_f32 v47, v47, s11, -v86
	v_exp_f32_e32 v46, v46
	v_cndmask_b32_e64 v44, 0, v44, s[80:81]
	v_add_f32_e32 v87, v87, v43
	v_cvt_pk_bf16_f32 v194, v42, v43
	v_add_f32_e32 v49, v49, v147
	v_fma_f32 v48, v48, s11, -v86
	v_exp_f32_e32 v47, v47
	v_cndmask_b32_e64 v45, 0, v45, s[82:83]
	v_add_f32_e32 v87, v87, v44
	v_fma_f32 v49, v49, s11, -v86
	v_exp_f32_e32 v48, v48
	v_cndmask_b32_e64 v46, 0, v46, s[84:85]
	v_add_f32_e32 v87, v87, v45
	v_cvt_pk_bf16_f32 v195, v44, v45
	v_exp_f32_e32 v49, v49
	v_cndmask_b32_e64 v47, 0, v47, s[86:87]
	v_add_f32_e32 v87, v87, v46
	v_cndmask_b32_e64 v48, 0, v48, s[94:95]
	v_add_f32_e32 v87, v87, v47
	v_cvt_pk_bf16_f32 v196, v46, v47
	v_cndmask_b32_e32 v49, 0, v49, vcc
	v_add_f32_e32 v87, v87, v48
	v_add_f32_e32 v87, v87, v49
	v_cvt_pk_bf16_f32 v197, v48, v49
	s_nop 1
	v_mfma_f32_32x32x16_bf16 v[2:17], v[104:107], v[194:197], v[2:17]
	s_waitcnt vmcnt(4)
	v_mfma_f32_32x32x16_bf16 v[18:33], v[112:115], v[194:197], v[18:33]
	s_cmp_eq_u32 s14, s4
	s_cbranch_scc0 .LBB0_763
	s_branch .LBB0_765
.LBB0_764:
	v_mov_b32_e32 v2, 0
	v_mov_b32_e32 v16, v2
	v_mov_b32_e32 v17, v2
	v_mov_b32_e32 v3, v2
	v_mov_b32_e32 v4, v2
	v_mov_b32_e32 v5, v2
	v_mov_b32_e32 v6, v2
	v_mov_b32_e32 v7, v2
	v_mov_b32_e32 v8, v2
	v_mov_b32_e32 v9, v2
	v_mov_b32_e32 v10, v2
	v_mov_b32_e32 v11, v2
	v_mov_b32_e32 v12, v2
	v_mov_b32_e32 v13, v2
	v_mov_b32_e32 v14, v2
	v_mov_b32_e32 v15, v2
	v_mov_b64_e32 v[32:33], v[16:17]
	v_mov_b64_e32 v[30:31], v[14:15]
	v_mov_b64_e32 v[28:29], v[12:13]
	v_mov_b64_e32 v[26:27], v[10:11]
	v_mov_b64_e32 v[24:25], v[8:9]
	v_mov_b64_e32 v[22:23], v[6:7]
	v_mov_b64_e32 v[20:21], v[4:5]
	v_mov_b64_e32 v[18:19], v[2:3]
	v_mov_b32_e32 v87, v2
	s_lshl_b32 s8, s12, 4
	s_or_b32 s8, s8, s15
	s_mulk_i32 s8, 0x88
	s_addk_i32 s8, 0x80
	s_ashr_i32 s9, s8, 31
	s_lshl_b64 s[8:9], s[8:9], 12
	v_lshl_add_u64 v[198:199], v[70:71], 0, s[8:9]
	global_load_dwordx4 v[116:119], v[198:199], off
	global_load_dwordx4 v[120:123], v[198:199], off offset:1024
	global_load_dwordx4 v[124:127], v[198:199], off offset:2048
	global_load_dwordx4 v[128:131], v[198:199], off offset:3072

; template <bool BAND> ...
;     pg8::bf16x8 kf[4];
; #pragma unroll
;     for (int ks = 0; ks < 4; ++ks) kf[ks] = *(const pg8::bf16x8*)(p.Kb + ((size_t)keyrow0 * 4 + ks) * 512 + (hh * 32 + r) * 8);
;     pg8::bf16x8 vf[2][2];
; #pragma unroll
;     for (int nt = 0; nt < 2; ++nt)
; #pragma unroll
;         for (int s = 0; s < 2; ++s) vf[nt][s] = *(const pg8::bf16x8*)(vtp + ((nt * 2 + s) * 64 + hh * 32 + r) * 8);
;     f32x16 sacc;
; #pragma unroll
;     for (int i = 0; i < 16; ++i) sacc[i] = 0.f;
; #pragma unroll
;     for (int ks = 0; ks < 4; ++ks) sacc = __builtin_amdgcn_mfma_f32_32x32x16_bf16(kf[ks], qf[ks], sacc, 0, 0, 0);
;     float pv[16];
; #pragma unroll
;     for (int reg = 0; reg < 16; ++reg) {
;         float sc = sacc[reg];
;         if (BAND) {
;             const int kc = kc0 + (reg & 3) + 8 * (reg >> 2) + 4 * hh;
;             const bool valid = (unsigned)(kc - c0) < 16u;
;             const int bi = valid ? browoff + kc - q + 15 : 0;
;             sc += tab[bi];
;             pv[reg] = valid ? __builtin_amdgcn_exp2f(sc * 1.44269504f - mq) : 0.f;
;         } else pv[reg] = __builtin_amdgcn_exp2f(sc * 1.44269504f - mq);
;         l += pv[reg];
;     }
;     pg8::bf16x8 pf[2];
; #pragma unroll
;     for (int s = 0; s < 2; ++s) { const pg8::u32x4 w = {cvt_pk_bf16(pv[8 * s], pv[8 * s + 1]), cvt_pk_bf16(pv[8 * s + 2], pv[8 * s + 3]), cvt_pk_bf16(pv[8 * s + 4], pv[8 * s + 5]), cvt_pk_bf16(pv[8 * s + 6], pv[8 * s + 7])};
; __device__ __forceinline__ void ph_naattn(const Params& p, float* lds, int wg, int nwg) {
;     ...
;         for (int kt = 0; kt < 8; ++kt)
;             { const int tid_ = (b * 16 + h) * 136 + 128 + kt; na_tile<false>(p, tab, qf, tid_, p.VTl + (size_t)tid_ * 2048, TC, h, r, hh, 0, 0, 0, 0, mq, o0, o1, l); }
;         l += __shfl_xor(l, 32);
;         const float inv = 1.f / l;
;         bf16_t* dst = p.MIXb + (size_t)(qrow0 + r) * DM + 1024 + h * 64 + 4 * hh;
; #pragma unroll
;         for (int g4 = 0; g4 < 4; ++g4) {
;             uint2 w0, w1;
;             w0.x = cvt_pk_bf16(o0[4 * g4] * inv, o0[4 * g4 + 1] * inv); w0.y = cvt_pk_bf16(o0[4 * g4 + 2] * inv, o0[4 * g4 + 3] * inv);
;             w1.x = cvt_pk_bf16(o1[4 * g4] * inv, o1[4 * g4 + 1] * inv); w1.y = cvt_pk_bf16(o1[4 * g4 + 2] * inv, o1[4 * g4 + 3] * inv);
;             *(uint2*)(dst + 8 * g4) = w0; *(uint2*)(dst + 32 + 8 * g4) = w1;
;         }
.LBB0_766:
	v_lshl_add_u64 v[108:109], v[80:81], 0, s[4:5]
	global_load_dwordx4 v[100:103], v[108:109], off
	global_load_dwordx4 v[104:107], v[108:109], off offset:2048
	global_load_dwordx4 v[88:91], v[108:109], off offset:1024
	global_load_dwordx4 v[92:95], v[108:109], off offset:3072
	s_add_u32 s4, s4, 0x1000
	s_addc_u32 s5, s5, 0
	s_waitcnt vmcnt(7)
	v_mfma_f32_32x32x16_bf16 v[34:49], v[116:119], v[50:53], 0
	s_waitcnt vmcnt(6)
	v_mfma_f32_32x32x16_bf16 v[34:49], v[120:123], v[54:57], v[34:49]
	s_waitcnt vmcnt(5)
	v_mfma_f32_32x32x16_bf16 v[34:49], v[124:127], v[58:61], v[34:49]
	s_waitcnt vmcnt(4)
	v_mfma_f32_32x32x16_bf16 v[34:49], v[128:131], v[62:65], v[34:49]
	s_min_u32 s8, s4, 0x7000
	s_mov_b32 s9, 0
	v_lshl_add_u64 v[198:199], v[82:83], 0, s[8:9]
	global_load_dwordx4 v[116:119], v[198:199], off
	global_load_dwordx4 v[120:123], v[198:199], off offset:1024
	global_load_dwordx4 v[124:127], v[198:199], off offset:2048
	global_load_dwordx4 v[128:131], v[198:199], off offset:3072
	s_nop 4
	v_fma_f32 v34, v34, s11, -v86
	v_fma_f32 v35, v35, s11, -v86
	v_fma_f32 v36, v36, s11, -v86
	v_fma_f32 v37, v37, s11, -v86
	v_fma_f32 v38, v38, s11, -v86
	v_fma_f32 v39, v39, s11, -v86
	v_fma_f32 v40, v40, s11, -v86
	v_fma_f32 v41, v41, s11, -v86
	v_exp_f32_e32 v96, v34
	v_exp_f32_e32 v97, v35
	v_exp_f32_e32 v98, v36
	v_exp_f32_e32 v99, v37
	v_exp_f32_e32 v38, v38
	v_exp_f32_e32 v39, v39
	v_exp_f32_e32 v40, v40
	v_exp_f32_e32 v41, v41
	v_cvt_pk_bf16_f32 v34, v96, v97
	v_cvt_pk_bf16_f32 v35, v98, v99
	v_cvt_pk_bf16_f32 v36, v38, v39
	v_cvt_pk_bf16_f32 v37, v40, v41
	v_add_f32_e32 v87, v87, v96
	v_add_f32_e32 v87, v97, v87
	s_waitcnt vmcnt(7)
	v_mfma_f32_32x32x16_bf16 v[2:17], v[100:103], v[34:37], v[2:17]
	v_fma_f32 v42, v42, s11, -v86
	v_fma_f32 v43, v43, s11, -v86
	v_fma_f32 v44, v44, s11, -v86
	v_fma_f32 v45, v45, s11, -v86
	v_fma_f32 v46, v46, s11, -v86
	v_fma_f32 v47, v47, s11, -v86
	v_fma_f32 v48, v48, s11, -v86
	s_waitcnt vmcnt(6)
	v_mfma_f32_32x32x16_bf16 v[18:33], v[104:107], v[34:37], v[18:33]
	v_fma_f32 v49, v49, s11, -v86
	v_add_f32_e32 v87, v98, v87
	v_exp_f32_e32 v42, v42
	v_exp_f32_e32 v43, v43
	v_exp_f32_e32 v44, v44
	v_exp_f32_e32 v45, v45
	v_exp_f32_e32 v46, v46
	v_exp_f32_e32 v47, v47
	v_exp_f32_e32 v48, v48
	v_exp_f32_e32 v49, v49
	v_add_f32_e32 v87, v99, v87
	v_add_f32_e32 v38, v38, v87
	v_add_f32_e32 v38, v39, v38
	v_add_f32_e32 v38, v40, v38
	v_cvt_pk_bf16_f32 v34, v42, v43
	v_cvt_pk_bf16_f32 v35, v44, v45
	v_cvt_pk_bf16_f32 v36, v46, v47
	v_cvt_pk_bf16_f32 v37, v48, v49
	v_add_f32_e32 v38, v41, v38
	v_add_f32_e32 v38, v42, v38
	s_waitcnt vmcnt(5)
	v_mfma_f32_32x32x16_bf16 v[2:17], v[88:91], v[34:37], v[2:17]
	s_waitcnt vmcnt(4)
	v_mfma_f32_32x32x16_bf16 v[18:33], v[92:95], v[34:37], v[18:33]
	v_add_f32_e32 v34, v43, v38
	v_add_f32_e32 v34, v44, v34
	v_add_f32_e32 v34, v45, v34
	v_add_f32_e32 v34, v46, v34
	v_add_f32_e32 v34, v47, v34
	v_add_f32_e32 v34, v48, v34
	v_add_f32_e32 v87, v49, v34
	s_cmpk_eq_u32 s4, 0x8000
	s_cbranch_scc0 .LBB0_766
	ds_bpermute_b32 v36, v165, v87
	v_readlane_b32 s12, v247, 16
	v_lshlrev_b64 v[34:35], 12, v[78:79]
	v_readlane_b32 s22, v247, 26
	v_readlane_b32 s23, v247, 27
	s_waitcnt lgkmcnt(0)
	v_add_f32_e32 v36, v87, v36
	v_div_scale_f32 v37, s[4:5], v36, v36, 1.0
	v_rcp_f32_e32 v38, v37
	v_div_scale_f32 v39, vcc, 1.0, v36, 1.0
	s_lshl_b32 s6, s6, 1
	v_fma_f32 v40, -v37, v38, 1.0
	v_fmac_f32_e32 v38, v40, v38
	v_mul_f32_e32 v40, v39, v38
	v_fma_f32 v41, -v37, v40, v39
	v_fmac_f32_e32 v40, v41, v38
	v_fma_f32 v37, -v37, v40, v39
	v_div_fmas_f32 v37, v37, v38, v40
	v_div_fixup_f32 v36, v37, v36, 1.0
	v_lshl_add_u64 v[34:35], s[22:23], 0, v[34:35]
	v_pk_mul_f32 v[2:3], v[2:3], v[36:37] op_sel_hi:[1,0]
	v_pk_mul_f32 v[4:5], v[4:5], v[36:37] op_sel_hi:[1,0]
	v_lshl_add_u64 v[34:35], v[34:35], 0, s[6:7]
	v_cvt_pk_bf16_f32 v2, v2, v3
	v_cvt_pk_bf16_f32 v3, v4, v5
	v_pk_mul_f32 v[4:5], v[18:19], v[36:37] op_sel_hi:[1,0]
	v_pk_mul_f32 v[18:19], v[20:21], v[36:37] op_sel_hi:[1,0]
	v_lshl_add_u64 v[34:35], v[34:35], 0, v[66:67]
	v_cvt_pk_bf16_f32 v4, v4, v5
	v_cvt_pk_bf16_f32 v5, v18, v19
	global_store_dwordx2 v[34:35], v[2:3], off offset:2048
	global_store_dwordx2 v[34:35], v[4:5], off offset:2112
	v_pk_mul_f32 v[2:3], v[6:7], v[36:37] op_sel_hi:[1,0]
	v_pk_mul_f32 v[4:5], v[8:9], v[36:37] op_sel_hi:[1,0]
	v_cvt_pk_bf16_f32 v2, v2, v3
	v_cvt_pk_bf16_f32 v3, v4, v5
	v_pk_mul_f32 v[4:5], v[22:23], v[36:37] op_sel_hi:[1,0]
	v_pk_mul_f32 v[6:7], v[24:25], v[36:37] op_sel_hi:[1,0]
	v_cvt_pk_bf16_f32 v4, v4, v5
	v_cvt_pk_bf16_f32 v5, v6, v7
	global_store_dwordx2 v[34:35], v[2:3], off offset:2064
	global_store_dwordx2 v[34:35], v[4:5], off offset:2128
	v_pk_mul_f32 v[2:3], v[10:11], v[36:37] op_sel_hi:[1,0]
	v_pk_mul_f32 v[4:5], v[12:13], v[36:37] op_sel_hi:[1,0]
	v_cvt_pk_bf16_f32 v2, v2, v3
	v_cvt_pk_bf16_f32 v3, v4, v5
	v_pk_mul_f32 v[4:5], v[26:27], v[36:37] op_sel_hi:[1,0]
	v_pk_mul_f32 v[6:7], v[28:29], v[36:37] op_sel_hi:[1,0]
	v_cvt_pk_bf16_f32 v4, v4, v5
	v_cvt_pk_bf16_f32 v5, v6, v7
	global_store_dwordx2 v[34:35], v[2:3], off offset:2080
	global_store_dwordx2 v[34:35], v[4:5], off offset:2144
	v_pk_mul_f32 v[2:3], v[14:15], v[36:37] op_sel_hi:[1,0]
	v_pk_mul_f32 v[4:5], v[16:17], v[36:37] op_sel_hi:[1,0]
	v_cvt_pk_bf16_f32 v2, v2, v3
	v_cvt_pk_bf16_f32 v3, v4, v5
	v_pk_mul_f32 v[4:5], v[30:31], v[36:37] op_sel_hi:[1,0]
	v_pk_mul_f32 v[6:7], v[32:33], v[36:37] op_sel_hi:[1,0]
	s_add_i32 s2, s2, s88
	s_sub_i32 s10, s10, s88
	v_cvt_pk_bf16_f32 v4, v4, v5
	v_cvt_pk_bf16_f32 v5, v6, v7
	s_cmpk_gt_i32 s2, 0x10ff
	v_readlane_b32 s13, v247, 17
	v_readlane_b32 s14, v247, 18
	v_readlane_b32 s15, v247, 19
	v_readlane_b32 s16, v247, 20
	v_readlane_b32 s17, v247, 21
	v_readlane_b32 s18, v247, 22
	v_readlane_b32 s19, v247, 23
	v_readlane_b32 s20, v247, 24
	v_readlane_b32 s21, v247, 25
	v_readlane_b32 s24, v247, 28
	v_readlane_b32 s25, v247, 29
	v_readlane_b32 s26, v247, 30
	v_readlane_b32 s27, v247, 31
	global_store_dwordx2 v[34:35], v[2:3], off offset:2096
	global_store_dwordx2 v[34:35], v[4:5], off offset:2160
	s_cbranch_scc0 .LBB0_753
